# idle-WG weight conversion inside in-proj/out-proj: loads nt -> sc0 sc1 nt as well (on top of v51)
# baseline (speedup 1.0000x reference)
.LBB0_579:
	s_waitcnt vmcnt(0)
	v_add_u32_e32 v12, s13, v88
	v_add_u32_e32 v4, 0x45, v12
	v_ashrrev_i32_e32 v13, 31, v12
	v_ashrrev_i32_e32 v5, 31, v4
	v_lshlrev_b64 v[0:1], 13, v[12:13]
	v_lshlrev_b64 v[4:5], 13, v[4:5]
	v_lshl_add_u64 v[0:1], v[64:65], 0, v[0:1]
	v_lshl_add_u64 v[4:5], v[64:65], 0, v[4:5]
	global_load_dwordx4 v[48:51], v[0:1], off sc0 sc1 nt
	v_add_u32_e32 v8, 0x46, v12
	global_load_dwordx4 v[4:7], v[4:5], off sc0 sc1 nt
	v_or_b32_e32 v0, 1, v12
	v_ashrrev_i32_e32 v1, 31, v0
	v_ashrrev_i32_e32 v9, 31, v8
	v_lshlrev_b64 v[0:1], 13, v[0:1]
	v_lshlrev_b64 v[8:9], 13, v[8:9]
	v_lshl_add_u64 v[0:1], v[64:65], 0, v[0:1]
	v_lshl_add_u64 v[8:9], v[64:65], 0, v[8:9]
	global_load_dwordx4 v[52:55], v[0:1], off sc0 sc1 nt
	v_mov_b32_e32 v67, v173
	global_load_dwordx4 v[8:11], v[8:9], off sc0 sc1 nt
	v_or_b32_e32 v0, 2, v12
	v_ashrrev_i32_e32 v1, 31, v0
	v_lshlrev_b64 v[0:1], 13, v[0:1]
	v_lshl_add_u64 v[0:1], v[64:65], 0, v[0:1]
	global_load_dwordx4 v[56:59], v[0:1], off sc0 sc1 nt
	v_or_b32_e32 v0, 3, v12
	v_ashrrev_i32_e32 v1, 31, v0
	v_lshlrev_b64 v[0:1], 13, v[0:1]
	v_lshl_add_u64 v[0:1], v[64:65], 0, v[0:1]
	global_load_dwordx4 v[60:63], v[0:1], off sc0 sc1 nt
	v_or_b32_e32 v0, 4, v12
	v_ashrrev_i32_e32 v1, 31, v0
	v_lshlrev_b64 v[0:1], 13, v[0:1]
	v_lshl_add_u64 v[0:1], v[64:65], 0, v[0:1]
	global_load_dwordx4 v[32:35], v[0:1], off sc0 sc1 nt
	v_or_b32_e32 v0, 5, v12
	v_ashrrev_i32_e32 v1, 31, v0
	v_lshlrev_b64 v[0:1], 13, v[0:1]
	v_lshl_add_u64 v[0:1], v[64:65], 0, v[0:1]
	global_load_dwordx4 v[36:39], v[0:1], off sc0 sc1 nt
	v_or_b32_e32 v0, 6, v12
	v_ashrrev_i32_e32 v1, 31, v0
	v_lshlrev_b64 v[0:1], 13, v[0:1]
	v_lshl_add_u64 v[0:1], v[64:65], 0, v[0:1]
	global_load_dwordx4 v[40:43], v[0:1], off sc0 sc1 nt
	v_or_b32_e32 v0, 7, v12
	v_ashrrev_i32_e32 v1, 31, v0
	v_lshlrev_b64 v[0:1], 13, v[0:1]
	v_lshl_add_u64 v[0:1], v[64:65], 0, v[0:1]
	global_load_dwordx4 v[44:47], v[0:1], off sc0 sc1 nt
	v_add_u32_e32 v0, 64, v12
	v_ashrrev_i32_e32 v1, 31, v0
	v_lshlrev_b64 v[0:1], 13, v[0:1]
	v_lshl_add_u64 v[0:1], v[64:65], 0, v[0:1]
	global_load_dwordx4 v[16:19], v[0:1], off sc0 sc1 nt
	v_add_u32_e32 v0, 0x41, v12
	v_ashrrev_i32_e32 v1, 31, v0
	v_lshlrev_b64 v[0:1], 13, v[0:1]
	v_lshl_add_u64 v[0:1], v[64:65], 0, v[0:1]
	global_load_dwordx4 v[20:23], v[0:1], off sc0 sc1 nt
	v_add_u32_e32 v0, 0x42, v12
	v_ashrrev_i32_e32 v1, 31, v0
	v_lshlrev_b64 v[0:1], 13, v[0:1]
	v_lshl_add_u64 v[0:1], v[64:65], 0, v[0:1]
	global_load_dwordx4 v[24:27], v[0:1], off sc0 sc1 nt
	v_add_u32_e32 v0, 0x43, v12
	v_ashrrev_i32_e32 v1, 31, v0
	v_lshlrev_b64 v[0:1], 13, v[0:1]
	v_lshl_add_u64 v[0:1], v[64:65], 0, v[0:1]
	global_load_dwordx4 v[28:31], v[0:1], off sc0 sc1 nt
	v_add_u32_e32 v0, 0x44, v12
	v_ashrrev_i32_e32 v1, 31, v0
	v_lshlrev_b64 v[0:1], 13, v[0:1]
	v_lshl_add_u64 v[0:1], v[64:65], 0, v[0:1]
	global_load_dwordx4 v[0:3], v[0:1], off sc0 sc1 nt
	v_add_u32_e32 v12, 0x47, v12
	v_ashrrev_i32_e32 v13, 31, v12
	v_lshlrev_b64 v[12:13], 13, v[12:13]
	v_lshl_add_u64 v[12:13], v[64:65], 0, v[12:13]
	global_load_dwordx4 v[12:15], v[12:13], off sc0 sc1 nt
	v_mov_b32_e32 v66, v173
	s_and_b64 vcc, exec, s[10:11]
	s_mov_b64 s[10:11], 0
	s_waitcnt vmcnt(15)
	v_mul_f32_e32 v48, 0x42000000, v48
	s_waitcnt vmcnt(14)
	v_mul_f32_e32 v4, 0x42000000, v4
	v_mul_f32_e32 v5, 0x42000000, v5
	s_waitcnt vmcnt(13)
	v_mul_f32_e32 v52, 0x42000000, v52
	v_cvt_pk_fp8_f32 v66, v48, v52
	s_waitcnt vmcnt(12)
	v_mul_f32_e32 v8, 0x42000000, v8
	s_waitcnt vmcnt(11)
	v_mul_f32_e32 v48, 0x42000000, v57
	v_mul_f32_e32 v56, 0x42000000, v56
	s_waitcnt vmcnt(10)
	v_mul_f32_e32 v60, 0x42000000, v60
	v_cvt_pk_fp8_f32 v66, v56, v60 op_sel:[0,0,1]
	s_waitcnt vmcnt(9)
	v_mul_f32_e32 v32, 0x42000000, v32
	s_waitcnt vmcnt(8)
	v_mul_f32_e32 v36, 0x42000000, v36
	v_cvt_pk_fp8_f32 v67, v32, v36
	v_mul_f32_e32 v32, 0x42000000, v49
	v_mul_f32_e32 v36, 0x42000000, v53
	v_mul_f32_e32 v49, 0x42000000, v61
	s_waitcnt vmcnt(7)
	v_mul_f32_e32 v40, 0x42000000, v40
	s_waitcnt vmcnt(6)
	v_mul_f32_e32 v44, 0x42000000, v44
	v_cvt_pk_fp8_f32 v67, v40, v44 op_sel:[0,0,1]
	v_mov_b32_e32 v40, v173
	v_cvt_pk_fp8_f32 v40, v32, v36
	v_mul_f32_e32 v32, 0x42000000, v33
	v_mul_f32_e32 v33, 0x42000000, v37
	v_mul_f32_e32 v36, 0x42000000, v41
	v_mov_b32_e32 v41, v173
	v_cvt_pk_fp8_f32 v41, v32, v33
	v_mul_f32_e32 v37, 0x42000000, v45
	v_mul_f32_e32 v32, 0x42000000, v50
	v_mul_f32_e32 v33, 0x42000000, v54
	v_cvt_pk_fp8_f32 v41, v36, v37 op_sel:[0,0,1]
	v_mov_b32_e32 v36, v173
	v_cvt_pk_fp8_f32 v36, v32, v33
	v_mul_f32_e32 v37, 0x42000000, v58
	v_mul_f32_e32 v45, 0x42000000, v62
	v_mul_f32_e32 v32, 0x42000000, v34
	v_cvt_pk_fp8_f32 v36, v37, v45 op_sel:[0,0,1]
	v_mul_f32_e32 v33, 0x42000000, v38
	v_mov_b32_e32 v37, v173
	v_cvt_pk_fp8_f32 v37, v32, v33
	v_mul_f32_e32 v34, 0x42000000, v42
	v_mul_f32_e32 v38, 0x42000000, v46
	v_mul_f32_e32 v33, 0x42000000, v51
	v_cvt_pk_fp8_f32 v37, v34, v38 op_sel:[0,0,1]
	v_mul_f32_e32 v34, 0x42000000, v55
	v_mov_b32_e32 v32, v173
	v_cvt_pk_fp8_f32 v32, v33, v34
	v_mul_f32_e32 v34, 0x42000000, v35
	v_mul_f32_e32 v35, 0x42000000, v39
	v_mov_b32_e32 v33, v173
	v_cvt_pk_fp8_f32 v33, v34, v35
	s_waitcnt vmcnt(1)
	v_mul_f32_e32 v0, 0x42000000, v0
	v_mov_b32_e32 v35, v173
	v_cvt_pk_fp8_f32 v35, v0, v4
	s_waitcnt vmcnt(0)
	v_mul_f32_e32 v12, 0x42000000, v12
	v_mul_f32_e32 v4, 0x42000000, v17
	v_mov_b32_e32 v0, v173
	v_cvt_pk_fp8_f32 v35, v8, v12 op_sel:[0,0,1]
	v_mul_f32_e32 v8, 0x42000000, v21
	v_cvt_pk_fp8_f32 v0, v4, v8
	v_mul_f32_e32 v4, 0x42000000, v1
	v_mov_b32_e32 v1, v173
	v_cvt_pk_fp8_f32 v1, v4, v5
	v_mul_f32_e32 v16, 0x42000000, v16
	v_mul_f32_e32 v20, 0x42000000, v20
	v_mov_b32_e32 v34, v173
	v_cvt_pk_fp8_f32 v34, v16, v20
	v_mul_f32_e32 v12, 0x42000000, v25
	v_mul_f32_e32 v16, 0x42000000, v29
	v_mul_f32_e32 v8, 0x42000000, v9
	v_mul_f32_e32 v9, 0x42000000, v13
	v_cvt_pk_fp8_f32 v40, v48, v49 op_sel:[0,0,1]
	v_cvt_pk_fp8_f32 v0, v12, v16 op_sel:[0,0,1]
	v_cvt_pk_fp8_f32 v1, v8, v9 op_sel:[0,0,1]
	v_add_u32_e32 v44, s13, v76
	v_mul_f32_e32 v4, 0x42000000, v22
	v_mul_f32_e32 v2, 0x42000000, v2
	ds_write2_b64 v44, v[40:41], v[0:1] offset0:34 offset1:42
	v_mul_f32_e32 v1, 0x42000000, v18
	v_mov_b32_e32 v0, v173
	v_cvt_pk_fp8_f32 v0, v1, v4
	v_mul_f32_e32 v4, 0x42000000, v6
	v_mov_b32_e32 v1, v173
	v_cvt_pk_fp8_f32 v1, v2, v4
	v_mul_f32_e32 v5, 0x42000000, v26
	v_mul_f32_e32 v8, 0x42000000, v30
	v_cvt_pk_fp8_f32 v0, v5, v8 op_sel:[0,0,1]
	v_mul_f32_e32 v5, 0x42000000, v10
	v_mul_f32_e32 v6, 0x42000000, v14
	v_cvt_pk_fp8_f32 v1, v5, v6 op_sel:[0,0,1]
	v_mul_f32_e32 v2, 0x42000000, v23
	v_mul_f32_e32 v38, 0x42000000, v59
	v_mul_f32_e32 v42, 0x42000000, v63
	ds_write2_b64 v44, v[36:37], v[0:1] offset0:68 offset1:76
	v_mul_f32_e32 v1, 0x42000000, v19
	v_mov_b32_e32 v0, v173
	v_cvt_pk_fp8_f32 v0, v1, v2
	v_mul_f32_e32 v2, 0x42000000, v3
	v_mul_f32_e32 v3, 0x42000000, v7
	v_mov_b32_e32 v1, v173
	v_cvt_pk_fp8_f32 v1, v2, v3
	v_mul_f32_e32 v4, 0x42000000, v27
	v_mul_f32_e32 v5, 0x42000000, v31
	v_cvt_pk_fp8_f32 v32, v38, v42 op_sel:[0,0,1]
	v_mul_f32_e32 v38, 0x42000000, v43
	v_mul_f32_e32 v39, 0x42000000, v47
	v_mul_f32_e32 v24, 0x42000000, v24
	v_mul_f32_e32 v28, 0x42000000, v28
	v_cvt_pk_fp8_f32 v0, v4, v5 op_sel:[0,0,1]
	v_mul_f32_e32 v4, 0x42000000, v11
	v_mul_f32_e32 v5, 0x42000000, v15
	v_cvt_pk_fp8_f32 v33, v38, v39 op_sel:[0,0,1]
	v_cvt_pk_fp8_f32 v34, v24, v28 op_sel:[0,0,1]
	v_cvt_pk_fp8_f32 v1, v4, v5 op_sel:[0,0,1]
	s_movk_i32 s13, 0x80
	ds_write2_b64 v44, v[66:67], v[34:35] offset1:8
	ds_write2_b64 v44, v[32:33], v[0:1] offset0:102 offset1:110
	s_cbranch_vccnz .LBB0_579
	s_lshl_b64 s[8:9], s[8:9], 21
	s_add_u32 s8, s95, s8
	s_addc_u32 s9, s97, s9
	s_lshl_b32 s2, s2, 8
	s_waitcnt lgkmcnt(0)
	s_barrier
	v_add_u32_e32 v88, v80, v172
	s_ashr_i32 s10, s3, 31
	ds_read_b128 v[0:3], v88
	v_add_u32_e32 v4, s2, v75
	s_add_u32 s8, s8, s3
	v_ashrrev_i32_e32 v5, 31, v4
	s_addc_u32 s9, s9, s10
	v_lshlrev_b64 v[4:5], 10, v[4:5]
	v_lshl_add_u64 v[4:5], s[8:9], 0, v[4:5]
	v_lshl_add_u64 v[4:5], v[4:5], 0, v[172:173]
	v_add_u32_e32 v89, v81, v172
	s_waitcnt lgkmcnt(0)
	global_store_dwordx4 v[4:5], v[0:3], off sc1
	ds_read_b128 v[0:3], v89
	v_add_u32_e32 v4, s2, v74
	v_ashrrev_i32_e32 v5, 31, v4
	v_lshlrev_b64 v[4:5], 10, v[4:5]
	v_lshl_add_u64 v[4:5], s[8:9], 0, v[4:5]
	v_lshl_add_u64 v[4:5], v[4:5], 0, v[172:173]
	v_add_u32_e32 v90, v82, v172
	s_waitcnt lgkmcnt(0)
	global_store_dwordx4 v[4:5], v[0:3], off sc1
	ds_read_b128 v[0:3], v90
	v_add_u32_e32 v4, s2, v73
	v_ashrrev_i32_e32 v5, 31, v4
	v_lshlrev_b64 v[4:5], 10, v[4:5]
	v_lshl_add_u64 v[4:5], s[8:9], 0, v[4:5]
	v_lshl_add_u64 v[4:5], v[4:5], 0, v[172:173]
	v_add_u32_e32 v91, v83, v172
	s_waitcnt lgkmcnt(0)
	global_store_dwordx4 v[4:5], v[0:3], off sc1
	ds_read_b128 v[0:3], v91
	v_add_u32_e32 v4, s2, v72
	v_ashrrev_i32_e32 v5, 31, v4
	v_lshlrev_b64 v[4:5], 10, v[4:5]
	v_lshl_add_u64 v[4:5], s[8:9], 0, v[4:5]
	v_lshl_add_u64 v[4:5], v[4:5], 0, v[172:173]
	v_add_u32_e32 v92, v84, v172
	s_waitcnt lgkmcnt(0)
	global_store_dwordx4 v[4:5], v[0:3], off sc1
	ds_read_b128 v[0:3], v92
	v_add_u32_e32 v4, s2, v71
	v_ashrrev_i32_e32 v5, 31, v4
	v_lshlrev_b64 v[4:5], 10, v[4:5]
	v_lshl_add_u64 v[4:5], s[8:9], 0, v[4:5]
	v_lshl_add_u64 v[4:5], v[4:5], 0, v[172:173]
	v_add_u32_e32 v93, v85, v172
	s_waitcnt lgkmcnt(0)
	global_store_dwordx4 v[4:5], v[0:3], off sc1
	ds_read_b128 v[0:3], v93
	v_add_u32_e32 v4, s2, v70
	v_ashrrev_i32_e32 v5, 31, v4
	v_lshlrev_b64 v[4:5], 10, v[4:5]
	v_lshl_add_u64 v[4:5], s[8:9], 0, v[4:5]
	v_lshl_add_u64 v[4:5], v[4:5], 0, v[172:173]
	v_add_u32_e32 v94, v86, v172
	s_waitcnt lgkmcnt(0)
	global_store_dwordx4 v[4:5], v[0:3], off sc1
	ds_read_b128 v[0:3], v94
	v_add_u32_e32 v4, s2, v69
	v_ashrrev_i32_e32 v5, 31, v4
	v_lshlrev_b64 v[4:5], 10, v[4:5]
	v_lshl_add_u64 v[4:5], s[8:9], 0, v[4:5]
	v_lshl_add_u64 v[4:5], v[4:5], 0, v[172:173]
	v_add_u32_e32 v95, v87, v172
	s_waitcnt lgkmcnt(0)
	global_store_dwordx4 v[4:5], v[0:3], off sc1
	ds_read_b128 v[0:3], v95
	v_add_u32_e32 v4, s2, v68
	v_ashrrev_i32_e32 v5, 31, v4
	v_lshlrev_b64 v[4:5], 10, v[4:5]
	v_lshl_add_u64 v[4:5], s[8:9], 0, v[4:5]
	v_lshl_add_u64 v[4:5], v[4:5], 0, v[172:173]
	s_waitcnt lgkmcnt(0)
	global_store_dwordx4 v[4:5], v[0:3], off sc1
	s_waitcnt lgkmcnt(0)
	s_barrier
	s_movk_i32 s8, 0xff60
	s_mov_b64 s[2:3], 0
	s_and_b64 vcc, exec, s[6:7]
	s_cbranch_vccz .LBB0_578
	v_readlane_b32 s0, v250, 60
	s_add_i32 s2, s0, s1
	s_ashr_i32 s3, s2, 31
	v_readlane_b32 s8, v255, 19
	s_lshl_b64 s[4:5], s[2:3], 20
	s_lshl_b64 s[2:3], s[2:3], 22
	v_readlane_b32 s14, v255, 25
	v_readlane_b32 s0, v250, 61
	v_readlane_b32 s15, v255, 26
	s_add_u32 s2, s14, s2
	v_or_b32_e32 v0, s0, v77
	s_addc_u32 s3, s15, s3
	v_readlane_b32 s0, v250, 63
	v_ashrrev_i32_e32 v1, 31, v0
	v_lshl_add_u64 v[64:65], v[0:1], 2, s[2:3]
	v_add_u32_e32 v77, s0, v78
	s_mov_b32 s1, 0
	s_mov_b64 s[6:7], -1
	v_readlane_b32 s9, v255, 20
	v_readlane_b32 s10, v255, 21
	v_readlane_b32 s11, v255, 22
	v_readlane_b32 s12, v255, 23
	v_readlane_b32 s13, v255, 24
.LBB0_582:
	v_add_u32_e32 v12, s1, v77
	v_add_u32_e32 v4, 0x45, v12
	v_ashrrev_i32_e32 v13, 31, v12
	v_ashrrev_i32_e32 v5, 31, v4
	v_lshlrev_b64 v[0:1], 12, v[12:13]
	v_lshlrev_b64 v[4:5], 12, v[4:5]
	v_lshl_add_u64 v[0:1], v[64:65], 0, v[0:1]
	v_lshl_add_u64 v[4:5], v[64:65], 0, v[4:5]
	global_load_dwordx4 v[48:51], v[0:1], off sc0 sc1 nt
	v_add_u32_e32 v8, 0x46, v12
	global_load_dwordx4 v[4:7], v[4:5], off sc0 sc1 nt
	v_or_b32_e32 v0, 1, v12
	v_ashrrev_i32_e32 v1, 31, v0
	v_ashrrev_i32_e32 v9, 31, v8
	v_lshlrev_b64 v[0:1], 12, v[0:1]
	v_lshlrev_b64 v[8:9], 12, v[8:9]
	v_lshl_add_u64 v[0:1], v[64:65], 0, v[0:1]
	v_lshl_add_u64 v[8:9], v[64:65], 0, v[8:9]
	global_load_dwordx4 v[52:55], v[0:1], off sc0 sc1 nt
	v_mov_b32_e32 v67, v173
	global_load_dwordx4 v[8:11], v[8:9], off sc0 sc1 nt
	v_or_b32_e32 v0, 2, v12
	v_ashrrev_i32_e32 v1, 31, v0
	v_lshlrev_b64 v[0:1], 12, v[0:1]
	v_lshl_add_u64 v[0:1], v[64:65], 0, v[0:1]
	global_load_dwordx4 v[56:59], v[0:1], off sc0 sc1 nt
	v_or_b32_e32 v0, 3, v12
	v_ashrrev_i32_e32 v1, 31, v0
	v_lshlrev_b64 v[0:1], 12, v[0:1]
	v_lshl_add_u64 v[0:1], v[64:65], 0, v[0:1]
	global_load_dwordx4 v[60:63], v[0:1], off sc0 sc1 nt
	v_or_b32_e32 v0, 4, v12
	v_ashrrev_i32_e32 v1, 31, v0
	v_lshlrev_b64 v[0:1], 12, v[0:1]
	v_lshl_add_u64 v[0:1], v[64:65], 0, v[0:1]
	global_load_dwordx4 v[32:35], v[0:1], off sc0 sc1 nt
	v_or_b32_e32 v0, 5, v12
	v_ashrrev_i32_e32 v1, 31, v0
	v_lshlrev_b64 v[0:1], 12, v[0:1]
	v_lshl_add_u64 v[0:1], v[64:65], 0, v[0:1]
	global_load_dwordx4 v[36:39], v[0:1], off sc0 sc1 nt
	v_or_b32_e32 v0, 6, v12
	v_ashrrev_i32_e32 v1, 31, v0
	v_lshlrev_b64 v[0:1], 12, v[0:1]
	v_lshl_add_u64 v[0:1], v[64:65], 0, v[0:1]
	global_load_dwordx4 v[40:43], v[0:1], off sc0 sc1 nt
	v_or_b32_e32 v0, 7, v12
	v_ashrrev_i32_e32 v1, 31, v0
	v_lshlrev_b64 v[0:1], 12, v[0:1]
	v_lshl_add_u64 v[0:1], v[64:65], 0, v[0:1]
	global_load_dwordx4 v[44:47], v[0:1], off sc0 sc1 nt
	v_add_u32_e32 v0, 64, v12
	v_ashrrev_i32_e32 v1, 31, v0
	v_lshlrev_b64 v[0:1], 12, v[0:1]
	v_lshl_add_u64 v[0:1], v[64:65], 0, v[0:1]
	global_load_dwordx4 v[16:19], v[0:1], off sc0 sc1 nt
	v_add_u32_e32 v0, 0x41, v12
	v_ashrrev_i32_e32 v1, 31, v0
	v_lshlrev_b64 v[0:1], 12, v[0:1]
	v_lshl_add_u64 v[0:1], v[64:65], 0, v[0:1]
	global_load_dwordx4 v[20:23], v[0:1], off sc0 sc1 nt
	v_add_u32_e32 v0, 0x42, v12
	v_ashrrev_i32_e32 v1, 31, v0
	v_lshlrev_b64 v[0:1], 12, v[0:1]
	v_lshl_add_u64 v[0:1], v[64:65], 0, v[0:1]
	global_load_dwordx4 v[24:27], v[0:1], off sc0 sc1 nt
	v_add_u32_e32 v0, 0x43, v12
	v_ashrrev_i32_e32 v1, 31, v0
	v_lshlrev_b64 v[0:1], 12, v[0:1]
	v_lshl_add_u64 v[0:1], v[64:65], 0, v[0:1]
	global_load_dwordx4 v[28:31], v[0:1], off sc0 sc1 nt
	v_add_u32_e32 v0, 0x44, v12
	v_ashrrev_i32_e32 v1, 31, v0
	v_lshlrev_b64 v[0:1], 12, v[0:1]
	v_lshl_add_u64 v[0:1], v[64:65], 0, v[0:1]
	global_load_dwordx4 v[0:3], v[0:1], off sc0 sc1 nt
	v_add_u32_e32 v12, 0x47, v12
	v_ashrrev_i32_e32 v13, 31, v12
	v_lshlrev_b64 v[12:13], 12, v[12:13]
	v_lshl_add_u64 v[12:13], v[64:65], 0, v[12:13]
	global_load_dwordx4 v[12:15], v[12:13], off sc0 sc1 nt
	v_mov_b32_e32 v66, v173
	s_and_b64 vcc, exec, s[6:7]
	s_mov_b64 s[6:7], 0
	s_waitcnt vmcnt(15)
	v_mul_f32_e32 v48, 0x42000000, v48
	s_waitcnt vmcnt(14)
	v_mul_f32_e32 v4, 0x42000000, v4
	v_mul_f32_e32 v5, 0x42000000, v5
	s_waitcnt vmcnt(13)
	v_mul_f32_e32 v52, 0x42000000, v52
	v_cvt_pk_fp8_f32 v66, v48, v52
	s_waitcnt vmcnt(12)
	v_mul_f32_e32 v8, 0x42000000, v8
	s_waitcnt vmcnt(11)
	v_mul_f32_e32 v48, 0x42000000, v57
	v_mul_f32_e32 v56, 0x42000000, v56
	s_waitcnt vmcnt(10)
	v_mul_f32_e32 v60, 0x42000000, v60
	v_cvt_pk_fp8_f32 v66, v56, v60 op_sel:[0,0,1]
	s_waitcnt vmcnt(9)
	v_mul_f32_e32 v32, 0x42000000, v32
	s_waitcnt vmcnt(8)
	v_mul_f32_e32 v36, 0x42000000, v36
	v_cvt_pk_fp8_f32 v67, v32, v36
	v_mul_f32_e32 v32, 0x42000000, v49
	v_mul_f32_e32 v36, 0x42000000, v53
	v_mul_f32_e32 v49, 0x42000000, v61
	s_waitcnt vmcnt(7)
	v_mul_f32_e32 v40, 0x42000000, v40
	s_waitcnt vmcnt(6)
	v_mul_f32_e32 v44, 0x42000000, v44
	v_cvt_pk_fp8_f32 v67, v40, v44 op_sel:[0,0,1]
	v_mov_b32_e32 v40, v173
	v_cvt_pk_fp8_f32 v40, v32, v36
	v_mul_f32_e32 v32, 0x42000000, v33
	v_mul_f32_e32 v33, 0x42000000, v37
	v_mul_f32_e32 v36, 0x42000000, v41
	v_mov_b32_e32 v41, v173
	v_cvt_pk_fp8_f32 v41, v32, v33
	v_mul_f32_e32 v37, 0x42000000, v45
	v_mul_f32_e32 v32, 0x42000000, v50
	v_mul_f32_e32 v33, 0x42000000, v54
	v_cvt_pk_fp8_f32 v41, v36, v37 op_sel:[0,0,1]
	v_mov_b32_e32 v36, v173
	v_cvt_pk_fp8_f32 v36, v32, v33
	v_mul_f32_e32 v37, 0x42000000, v58
	v_mul_f32_e32 v45, 0x42000000, v62
	v_mul_f32_e32 v32, 0x42000000, v34
	v_cvt_pk_fp8_f32 v36, v37, v45 op_sel:[0,0,1]
	v_mul_f32_e32 v33, 0x42000000, v38
	v_mov_b32_e32 v37, v173
	v_cvt_pk_fp8_f32 v37, v32, v33
	v_mul_f32_e32 v34, 0x42000000, v42
	v_mul_f32_e32 v38, 0x42000000, v46
	v_mul_f32_e32 v33, 0x42000000, v51
	v_cvt_pk_fp8_f32 v37, v34, v38 op_sel:[0,0,1]
	v_mul_f32_e32 v34, 0x42000000, v55
	v_mov_b32_e32 v32, v173
	v_cvt_pk_fp8_f32 v32, v33, v34
	v_mul_f32_e32 v34, 0x42000000, v35
	v_mul_f32_e32 v35, 0x42000000, v39
	v_mov_b32_e32 v33, v173
	v_cvt_pk_fp8_f32 v33, v34, v35
	s_waitcnt vmcnt(1)
	v_mul_f32_e32 v0, 0x42000000, v0
	v_mov_b32_e32 v35, v173
	v_cvt_pk_fp8_f32 v35, v0, v4
	s_waitcnt vmcnt(0)
	v_mul_f32_e32 v12, 0x42000000, v12
	v_mul_f32_e32 v4, 0x42000000, v17
	v_mov_b32_e32 v0, v173
	v_cvt_pk_fp8_f32 v35, v8, v12 op_sel:[0,0,1]
	v_mul_f32_e32 v8, 0x42000000, v21
	v_cvt_pk_fp8_f32 v0, v4, v8
	v_mul_f32_e32 v4, 0x42000000, v1
	v_mov_b32_e32 v1, v173
	v_cvt_pk_fp8_f32 v1, v4, v5
	v_mul_f32_e32 v16, 0x42000000, v16
	v_mul_f32_e32 v20, 0x42000000, v20
	v_mov_b32_e32 v34, v173
	v_cvt_pk_fp8_f32 v34, v16, v20
	v_mul_f32_e32 v12, 0x42000000, v25
	v_mul_f32_e32 v16, 0x42000000, v29
	v_mul_f32_e32 v8, 0x42000000, v9
	v_mul_f32_e32 v9, 0x42000000, v13
	v_cvt_pk_fp8_f32 v40, v48, v49 op_sel:[0,0,1]
	v_cvt_pk_fp8_f32 v0, v12, v16 op_sel:[0,0,1]
	v_cvt_pk_fp8_f32 v1, v8, v9 op_sel:[0,0,1]
	v_add_u32_e32 v44, s1, v76
	v_mul_f32_e32 v4, 0x42000000, v22
	v_mul_f32_e32 v2, 0x42000000, v2
	ds_write2_b64 v44, v[40:41], v[0:1] offset0:34 offset1:42
	v_mul_f32_e32 v1, 0x42000000, v18
	v_mov_b32_e32 v0, v173
	v_cvt_pk_fp8_f32 v0, v1, v4
	v_mul_f32_e32 v4, 0x42000000, v6
	v_mov_b32_e32 v1, v173
	v_cvt_pk_fp8_f32 v1, v2, v4
	v_mul_f32_e32 v5, 0x42000000, v26
	v_mul_f32_e32 v8, 0x42000000, v30
	v_cvt_pk_fp8_f32 v0, v5, v8 op_sel:[0,0,1]
	v_mul_f32_e32 v5, 0x42000000, v10
	v_mul_f32_e32 v6, 0x42000000, v14
	v_cvt_pk_fp8_f32 v1, v5, v6 op_sel:[0,0,1]
	v_mul_f32_e32 v2, 0x42000000, v23
	v_mul_f32_e32 v38, 0x42000000, v59
	v_mul_f32_e32 v42, 0x42000000, v63
	ds_write2_b64 v44, v[36:37], v[0:1] offset0:68 offset1:76
	v_mul_f32_e32 v1, 0x42000000, v19
	v_mov_b32_e32 v0, v173
	v_cvt_pk_fp8_f32 v0, v1, v2
	v_mul_f32_e32 v2, 0x42000000, v3
	v_mul_f32_e32 v3, 0x42000000, v7
	v_mov_b32_e32 v1, v173
	v_cvt_pk_fp8_f32 v1, v2, v3
	v_mul_f32_e32 v4, 0x42000000, v27
	v_mul_f32_e32 v5, 0x42000000, v31
	v_cvt_pk_fp8_f32 v32, v38, v42 op_sel:[0,0,1]
	v_mul_f32_e32 v38, 0x42000000, v43
	v_mul_f32_e32 v39, 0x42000000, v47
	v_mul_f32_e32 v24, 0x42000000, v24
	v_mul_f32_e32 v28, 0x42000000, v28
	v_cvt_pk_fp8_f32 v0, v4, v5 op_sel:[0,0,1]
	v_mul_f32_e32 v4, 0x42000000, v11
	v_mul_f32_e32 v5, 0x42000000, v15
	v_cvt_pk_fp8_f32 v33, v38, v39 op_sel:[0,0,1]
	v_cvt_pk_fp8_f32 v34, v24, v28 op_sel:[0,0,1]
	v_cvt_pk_fp8_f32 v1, v4, v5 op_sel:[0,0,1]
	s_movk_i32 s1, 0x80
	ds_write2_b64 v44, v[66:67], v[34:35] offset1:8
	ds_write2_b64 v44, v[32:33], v[0:1] offset0:102 offset1:110
	s_cbranch_vccnz .LBB0_582
	v_readlane_b32 s0, v251, 0
	s_add_u32 s2, s0, s4
	v_readlane_b32 s0, v251, 2
	s_waitcnt lgkmcnt(0)
	s_barrier
	s_addc_u32 s3, s0, s5
	v_readlane_b32 s0, v250, 61
	ds_read_b128 v[0:3], v88
	s_nop 0
	v_add_u32_e32 v4, s0, v75
	v_ashrrev_i32_e32 v5, 31, v4
	v_lshlrev_b64 v[4:5], 10, v[4:5]
	v_lshl_add_u64 v[4:5], s[2:3], 0, v[4:5]
	v_lshl_add_u64 v[4:5], v[4:5], 0, v[172:173]
	s_waitcnt lgkmcnt(0)
	global_store_dwordx4 v[4:5], v[0:3], off sc1
	ds_read_b128 v[0:3], v89
	v_add_u32_e32 v4, s0, v74
	v_ashrrev_i32_e32 v5, 31, v4
	v_lshlrev_b64 v[4:5], 10, v[4:5]
	v_lshl_add_u64 v[4:5], s[2:3], 0, v[4:5]
	v_lshl_add_u64 v[4:5], v[4:5], 0, v[172:173]
	s_waitcnt lgkmcnt(0)
	global_store_dwordx4 v[4:5], v[0:3], off sc1
	ds_read_b128 v[0:3], v90
	v_add_u32_e32 v4, s0, v73
	v_ashrrev_i32_e32 v5, 31, v4
	v_lshlrev_b64 v[4:5], 10, v[4:5]
	v_lshl_add_u64 v[4:5], s[2:3], 0, v[4:5]
	v_lshl_add_u64 v[4:5], v[4:5], 0, v[172:173]
	s_waitcnt lgkmcnt(0)
	global_store_dwordx4 v[4:5], v[0:3], off sc1
	ds_read_b128 v[0:3], v91
	v_add_u32_e32 v4, s0, v72
	v_ashrrev_i32_e32 v5, 31, v4
	v_lshlrev_b64 v[4:5], 10, v[4:5]
	v_lshl_add_u64 v[4:5], s[2:3], 0, v[4:5]
	v_lshl_add_u64 v[4:5], v[4:5], 0, v[172:173]
	s_waitcnt lgkmcnt(0)
	global_store_dwordx4 v[4:5], v[0:3], off sc1
	ds_read_b128 v[0:3], v92
	v_add_u32_e32 v4, s0, v71
	v_ashrrev_i32_e32 v5, 31, v4
	v_lshlrev_b64 v[4:5], 10, v[4:5]
	v_lshl_add_u64 v[4:5], s[2:3], 0, v[4:5]
	v_lshl_add_u64 v[4:5], v[4:5], 0, v[172:173]
	s_waitcnt lgkmcnt(0)
	global_store_dwordx4 v[4:5], v[0:3], off sc1
	ds_read_b128 v[0:3], v93
	v_add_u32_e32 v4, s0, v70
	v_ashrrev_i32_e32 v5, 31, v4
	v_lshlrev_b64 v[4:5], 10, v[4:5]
	v_lshl_add_u64 v[4:5], s[2:3], 0, v[4:5]
	v_lshl_add_u64 v[4:5], v[4:5], 0, v[172:173]
	s_waitcnt lgkmcnt(0)
	global_store_dwordx4 v[4:5], v[0:3], off sc1
	ds_read_b128 v[0:3], v94
	v_add_u32_e32 v4, s0, v69
	v_ashrrev_i32_e32 v5, 31, v4
	v_lshlrev_b64 v[4:5], 10, v[4:5]
	v_lshl_add_u64 v[4:5], s[2:3], 0, v[4:5]
	v_lshl_add_u64 v[4:5], v[4:5], 0, v[172:173]
	s_waitcnt lgkmcnt(0)
	global_store_dwordx4 v[4:5], v[0:3], off sc1
	ds_read_b128 v[0:3], v95
	v_add_u32_e32 v4, s0, v68
	v_ashrrev_i32_e32 v5, 31, v4
	v_lshlrev_b64 v[4:5], 10, v[4:5]
	v_lshl_add_u64 v[4:5], s[2:3], 0, v[4:5]
	v_lshl_add_u64 v[4:5], v[4:5], 0, v[172:173]
	s_waitcnt lgkmcnt(0)
	global_store_dwordx4 v[4:5], v[0:3], off sc1
	s_waitcnt lgkmcnt(0)
	s_barrier

.LBB0_1328:
	v_add_u32_e32 v12, s12, v88
	v_add_u32_e32 v4, 0x45, v12
	v_ashrrev_i32_e32 v13, 31, v12
	v_ashrrev_i32_e32 v5, 31, v4
	v_lshlrev_b64 v[0:1], 13, v[12:13]
	v_lshlrev_b64 v[4:5], 13, v[4:5]
	v_lshl_add_u64 v[0:1], v[64:65], 0, v[0:1]
	v_lshl_add_u64 v[4:5], v[64:65], 0, v[4:5]
	global_load_dwordx4 v[48:51], v[0:1], off sc0 sc1 nt
	v_add_u32_e32 v8, 0x46, v12
	global_load_dwordx4 v[4:7], v[4:5], off sc0 sc1 nt
	v_or_b32_e32 v0, 1, v12
	v_ashrrev_i32_e32 v1, 31, v0
	v_ashrrev_i32_e32 v9, 31, v8
	v_lshlrev_b64 v[0:1], 13, v[0:1]
	v_lshlrev_b64 v[8:9], 13, v[8:9]
	v_lshl_add_u64 v[0:1], v[64:65], 0, v[0:1]
	v_lshl_add_u64 v[8:9], v[64:65], 0, v[8:9]
	global_load_dwordx4 v[52:55], v[0:1], off sc0 sc1 nt
	v_mov_b32_e32 v67, v173
	global_load_dwordx4 v[8:11], v[8:9], off sc0 sc1 nt
	v_or_b32_e32 v0, 2, v12
	v_ashrrev_i32_e32 v1, 31, v0
	v_lshlrev_b64 v[0:1], 13, v[0:1]
	v_lshl_add_u64 v[0:1], v[64:65], 0, v[0:1]
	global_load_dwordx4 v[56:59], v[0:1], off sc0 sc1 nt
	v_or_b32_e32 v0, 3, v12
	v_ashrrev_i32_e32 v1, 31, v0
	v_lshlrev_b64 v[0:1], 13, v[0:1]
	v_lshl_add_u64 v[0:1], v[64:65], 0, v[0:1]
	global_load_dwordx4 v[60:63], v[0:1], off sc0 sc1 nt
	v_or_b32_e32 v0, 4, v12
	v_ashrrev_i32_e32 v1, 31, v0
	v_lshlrev_b64 v[0:1], 13, v[0:1]
	v_lshl_add_u64 v[0:1], v[64:65], 0, v[0:1]
	global_load_dwordx4 v[32:35], v[0:1], off sc0 sc1 nt
	v_or_b32_e32 v0, 5, v12
	v_ashrrev_i32_e32 v1, 31, v0
	v_lshlrev_b64 v[0:1], 13, v[0:1]
	v_lshl_add_u64 v[0:1], v[64:65], 0, v[0:1]
	global_load_dwordx4 v[36:39], v[0:1], off sc0 sc1 nt
	v_or_b32_e32 v0, 6, v12
	v_ashrrev_i32_e32 v1, 31, v0
	v_lshlrev_b64 v[0:1], 13, v[0:1]
	v_lshl_add_u64 v[0:1], v[64:65], 0, v[0:1]
	global_load_dwordx4 v[40:43], v[0:1], off sc0 sc1 nt
	v_or_b32_e32 v0, 7, v12
	v_ashrrev_i32_e32 v1, 31, v0
	v_lshlrev_b64 v[0:1], 13, v[0:1]
	v_lshl_add_u64 v[0:1], v[64:65], 0, v[0:1]
	global_load_dwordx4 v[44:47], v[0:1], off sc0 sc1 nt
	v_add_u32_e32 v0, 64, v12
	v_ashrrev_i32_e32 v1, 31, v0
	v_lshlrev_b64 v[0:1], 13, v[0:1]
	v_lshl_add_u64 v[0:1], v[64:65], 0, v[0:1]
	global_load_dwordx4 v[16:19], v[0:1], off sc0 sc1 nt
	v_add_u32_e32 v0, 0x41, v12
	v_ashrrev_i32_e32 v1, 31, v0
	v_lshlrev_b64 v[0:1], 13, v[0:1]
	v_lshl_add_u64 v[0:1], v[64:65], 0, v[0:1]
	global_load_dwordx4 v[20:23], v[0:1], off sc0 sc1 nt
	v_add_u32_e32 v0, 0x42, v12
	v_ashrrev_i32_e32 v1, 31, v0
	v_lshlrev_b64 v[0:1], 13, v[0:1]
	v_lshl_add_u64 v[0:1], v[64:65], 0, v[0:1]
	global_load_dwordx4 v[24:27], v[0:1], off sc0 sc1 nt
	v_add_u32_e32 v0, 0x43, v12
	v_ashrrev_i32_e32 v1, 31, v0
	v_lshlrev_b64 v[0:1], 13, v[0:1]
	v_lshl_add_u64 v[0:1], v[64:65], 0, v[0:1]
	global_load_dwordx4 v[28:31], v[0:1], off sc0 sc1 nt
	v_add_u32_e32 v0, 0x44, v12
	v_ashrrev_i32_e32 v1, 31, v0
	v_lshlrev_b64 v[0:1], 13, v[0:1]
	v_lshl_add_u64 v[0:1], v[64:65], 0, v[0:1]
	global_load_dwordx4 v[0:3], v[0:1], off sc0 sc1 nt
	v_add_u32_e32 v12, 0x47, v12
	v_ashrrev_i32_e32 v13, 31, v12
	v_lshlrev_b64 v[12:13], 13, v[12:13]
	v_lshl_add_u64 v[12:13], v[64:65], 0, v[12:13]
	global_load_dwordx4 v[12:15], v[12:13], off sc0 sc1 nt
	v_mov_b32_e32 v66, v173
	s_and_b64 vcc, exec, s[10:11]
	s_mov_b64 s[10:11], 0
	s_waitcnt vmcnt(15)
	v_mul_f32_e32 v48, 0x42000000, v48
	s_waitcnt vmcnt(14)
	v_mul_f32_e32 v4, 0x42000000, v4
	v_mul_f32_e32 v5, 0x42000000, v5
	s_waitcnt vmcnt(13)
	v_mul_f32_e32 v52, 0x42000000, v52
	v_cvt_pk_fp8_f32 v66, v48, v52
	s_waitcnt vmcnt(12)
	v_mul_f32_e32 v8, 0x42000000, v8
	s_waitcnt vmcnt(11)
	v_mul_f32_e32 v48, 0x42000000, v57
	v_mul_f32_e32 v56, 0x42000000, v56
	s_waitcnt vmcnt(10)
	v_mul_f32_e32 v60, 0x42000000, v60
	v_cvt_pk_fp8_f32 v66, v56, v60 op_sel:[0,0,1]
	s_waitcnt vmcnt(9)
	v_mul_f32_e32 v32, 0x42000000, v32
	s_waitcnt vmcnt(8)
	v_mul_f32_e32 v36, 0x42000000, v36
	v_cvt_pk_fp8_f32 v67, v32, v36
	v_mul_f32_e32 v32, 0x42000000, v49
	v_mul_f32_e32 v36, 0x42000000, v53
	v_mul_f32_e32 v49, 0x42000000, v61
	s_waitcnt vmcnt(7)
	v_mul_f32_e32 v40, 0x42000000, v40
	s_waitcnt vmcnt(6)
	v_mul_f32_e32 v44, 0x42000000, v44
	v_cvt_pk_fp8_f32 v67, v40, v44 op_sel:[0,0,1]
	v_mov_b32_e32 v40, v173
	v_cvt_pk_fp8_f32 v40, v32, v36
	v_mul_f32_e32 v32, 0x42000000, v33
	v_mul_f32_e32 v33, 0x42000000, v37
	v_mul_f32_e32 v36, 0x42000000, v41
	v_mov_b32_e32 v41, v173
	v_cvt_pk_fp8_f32 v41, v32, v33
	v_mul_f32_e32 v37, 0x42000000, v45
	v_mul_f32_e32 v32, 0x42000000, v50
	v_mul_f32_e32 v33, 0x42000000, v54
	v_cvt_pk_fp8_f32 v41, v36, v37 op_sel:[0,0,1]
	v_mov_b32_e32 v36, v173
	v_cvt_pk_fp8_f32 v36, v32, v33
	v_mul_f32_e32 v37, 0x42000000, v58
	v_mul_f32_e32 v45, 0x42000000, v62
	v_mul_f32_e32 v32, 0x42000000, v34
	v_cvt_pk_fp8_f32 v36, v37, v45 op_sel:[0,0,1]
	v_mul_f32_e32 v33, 0x42000000, v38
	v_mov_b32_e32 v37, v173
	v_cvt_pk_fp8_f32 v37, v32, v33
	v_mul_f32_e32 v34, 0x42000000, v42
	v_mul_f32_e32 v38, 0x42000000, v46
	v_mul_f32_e32 v33, 0x42000000, v51
	v_cvt_pk_fp8_f32 v37, v34, v38 op_sel:[0,0,1]
	v_mul_f32_e32 v34, 0x42000000, v55
	v_mov_b32_e32 v32, v173
	v_cvt_pk_fp8_f32 v32, v33, v34
	v_mul_f32_e32 v34, 0x42000000, v35
	v_mul_f32_e32 v35, 0x42000000, v39
	v_mov_b32_e32 v33, v173
	v_cvt_pk_fp8_f32 v33, v34, v35
	s_waitcnt vmcnt(1)
	v_mul_f32_e32 v0, 0x42000000, v0
	v_mov_b32_e32 v35, v173
	v_cvt_pk_fp8_f32 v35, v0, v4
	s_waitcnt vmcnt(0)
	v_mul_f32_e32 v12, 0x42000000, v12
	v_mul_f32_e32 v4, 0x42000000, v17
	v_mov_b32_e32 v0, v173
	v_cvt_pk_fp8_f32 v35, v8, v12 op_sel:[0,0,1]
	v_mul_f32_e32 v8, 0x42000000, v21
	v_cvt_pk_fp8_f32 v0, v4, v8
	v_mul_f32_e32 v4, 0x42000000, v1
	v_mov_b32_e32 v1, v173
	v_cvt_pk_fp8_f32 v1, v4, v5
	v_mul_f32_e32 v16, 0x42000000, v16
	v_mul_f32_e32 v20, 0x42000000, v20
	v_mov_b32_e32 v34, v173
	v_cvt_pk_fp8_f32 v34, v16, v20
	v_mul_f32_e32 v12, 0x42000000, v25
	v_mul_f32_e32 v16, 0x42000000, v29
	v_mul_f32_e32 v8, 0x42000000, v9
	v_mul_f32_e32 v9, 0x42000000, v13
	v_cvt_pk_fp8_f32 v40, v48, v49 op_sel:[0,0,1]
	v_cvt_pk_fp8_f32 v0, v12, v16 op_sel:[0,0,1]
	v_cvt_pk_fp8_f32 v1, v8, v9 op_sel:[0,0,1]
	v_add_u32_e32 v44, s12, v79
	v_mul_f32_e32 v4, 0x42000000, v22
	v_mul_f32_e32 v2, 0x42000000, v2
	ds_write2_b64 v44, v[40:41], v[0:1] offset0:34 offset1:42
	v_mul_f32_e32 v1, 0x42000000, v18
	v_mov_b32_e32 v0, v173
	v_cvt_pk_fp8_f32 v0, v1, v4
	v_mul_f32_e32 v4, 0x42000000, v6
	v_mov_b32_e32 v1, v173
	v_cvt_pk_fp8_f32 v1, v2, v4
	v_mul_f32_e32 v5, 0x42000000, v26
	v_mul_f32_e32 v8, 0x42000000, v30
	v_cvt_pk_fp8_f32 v0, v5, v8 op_sel:[0,0,1]
	v_mul_f32_e32 v5, 0x42000000, v10
	v_mul_f32_e32 v6, 0x42000000, v14
	v_cvt_pk_fp8_f32 v1, v5, v6 op_sel:[0,0,1]
	v_mul_f32_e32 v2, 0x42000000, v23
	v_mul_f32_e32 v38, 0x42000000, v59
	v_mul_f32_e32 v42, 0x42000000, v63
	ds_write2_b64 v44, v[36:37], v[0:1] offset0:68 offset1:76
	v_mul_f32_e32 v1, 0x42000000, v19
	v_mov_b32_e32 v0, v173
	v_cvt_pk_fp8_f32 v0, v1, v2
	v_mul_f32_e32 v2, 0x42000000, v3
	v_mul_f32_e32 v3, 0x42000000, v7
	v_mov_b32_e32 v1, v173
	v_cvt_pk_fp8_f32 v1, v2, v3
	v_mul_f32_e32 v4, 0x42000000, v27
	v_mul_f32_e32 v5, 0x42000000, v31
	v_cvt_pk_fp8_f32 v32, v38, v42 op_sel:[0,0,1]
	v_mul_f32_e32 v38, 0x42000000, v43
	v_mul_f32_e32 v39, 0x42000000, v47
	v_mul_f32_e32 v24, 0x42000000, v24
	v_mul_f32_e32 v28, 0x42000000, v28
	v_cvt_pk_fp8_f32 v0, v4, v5 op_sel:[0,0,1]
	v_mul_f32_e32 v4, 0x42000000, v11
	v_mul_f32_e32 v5, 0x42000000, v15
	v_cvt_pk_fp8_f32 v33, v38, v39 op_sel:[0,0,1]
	v_cvt_pk_fp8_f32 v34, v24, v28 op_sel:[0,0,1]
	v_cvt_pk_fp8_f32 v1, v4, v5 op_sel:[0,0,1]
	s_movk_i32 s12, 0x80
	ds_write2_b64 v44, v[66:67], v[34:35] offset1:8
	ds_write2_b64 v44, v[32:33], v[0:1] offset0:102 offset1:110
	s_cbranch_vccnz .LBB0_1328
	s_lshl_b64 s[8:9], s[8:9], 21
	s_add_u32 s8, s95, s8
	s_addc_u32 s9, s97, s9
	s_lshl_b32 s10, s2, 8
	s_waitcnt lgkmcnt(0)
	s_barrier
	s_ashr_i32 s11, s3, 31
	ds_read_b128 v[0:3], v80
	v_add_u32_e32 v4, s10, v71
	s_add_u32 s2, s8, s3
	v_ashrrev_i32_e32 v5, 31, v4
	s_addc_u32 s3, s9, s11
	v_lshlrev_b64 v[4:5], 10, v[4:5]
	v_lshl_add_u64 v[4:5], s[2:3], 0, v[4:5]
	v_lshl_add_u64 v[4:5], v[4:5], 0, v[172:173]
	s_waitcnt lgkmcnt(0)
	global_store_dwordx4 v[4:5], v[0:3], off sc1
	ds_read_b128 v[0:3], v81
	v_add_u32_e32 v4, s10, v72
	v_ashrrev_i32_e32 v5, 31, v4
	v_lshlrev_b64 v[4:5], 10, v[4:5]
	v_lshl_add_u64 v[4:5], s[2:3], 0, v[4:5]
	v_lshl_add_u64 v[4:5], v[4:5], 0, v[172:173]
	s_waitcnt lgkmcnt(0)
	global_store_dwordx4 v[4:5], v[0:3], off sc1
	ds_read_b128 v[0:3], v82
	v_add_u32_e32 v4, s10, v73
	v_ashrrev_i32_e32 v5, 31, v4
	v_lshlrev_b64 v[4:5], 10, v[4:5]
	v_lshl_add_u64 v[4:5], s[2:3], 0, v[4:5]
	v_lshl_add_u64 v[4:5], v[4:5], 0, v[172:173]
	s_waitcnt lgkmcnt(0)
	global_store_dwordx4 v[4:5], v[0:3], off sc1
	ds_read_b128 v[0:3], v83
	v_add_u32_e32 v4, s10, v74
	v_ashrrev_i32_e32 v5, 31, v4
	v_lshlrev_b64 v[4:5], 10, v[4:5]
	v_lshl_add_u64 v[4:5], s[2:3], 0, v[4:5]
	v_lshl_add_u64 v[4:5], v[4:5], 0, v[172:173]
	s_waitcnt lgkmcnt(0)
	global_store_dwordx4 v[4:5], v[0:3], off sc1
	ds_read_b128 v[0:3], v84
	v_add_u32_e32 v4, s10, v75
	v_ashrrev_i32_e32 v5, 31, v4
	v_lshlrev_b64 v[4:5], 10, v[4:5]
	v_lshl_add_u64 v[4:5], s[2:3], 0, v[4:5]
	v_lshl_add_u64 v[4:5], v[4:5], 0, v[172:173]
	s_waitcnt lgkmcnt(0)
	global_store_dwordx4 v[4:5], v[0:3], off sc1
	ds_read_b128 v[0:3], v85
	v_add_u32_e32 v4, s10, v76
	v_ashrrev_i32_e32 v5, 31, v4
	v_lshlrev_b64 v[4:5], 10, v[4:5]
	v_lshl_add_u64 v[4:5], s[2:3], 0, v[4:5]
	v_lshl_add_u64 v[4:5], v[4:5], 0, v[172:173]
	s_waitcnt lgkmcnt(0)
	global_store_dwordx4 v[4:5], v[0:3], off sc1
	ds_read_b128 v[0:3], v86
	v_add_u32_e32 v4, s10, v77
	v_ashrrev_i32_e32 v5, 31, v4
	v_lshlrev_b64 v[4:5], 10, v[4:5]
	v_lshl_add_u64 v[4:5], s[2:3], 0, v[4:5]
	v_lshl_add_u64 v[4:5], v[4:5], 0, v[172:173]
	s_waitcnt lgkmcnt(0)
	global_store_dwordx4 v[4:5], v[0:3], off sc1
	ds_read_b128 v[0:3], v87
	v_add_u32_e32 v4, s10, v78
	v_ashrrev_i32_e32 v5, 31, v4
	v_lshlrev_b64 v[4:5], 10, v[4:5]
	v_lshl_add_u64 v[4:5], s[2:3], 0, v[4:5]
	v_lshl_add_u64 v[4:5], v[4:5], 0, v[172:173]
	s_waitcnt lgkmcnt(0)
	global_store_dwordx4 v[4:5], v[0:3], off sc1
	s_waitcnt lgkmcnt(0)
	s_barrier
	s_movk_i32 s8, 0xc0
	s_mov_b64 s[2:3], 0
	s_andn2_b64 vcc, exec, s[6:7]
	s_cbranch_vccnz .LBB0_1327
